# baseline (speedup 1.0000x reference)
.LBB13_6:
	s_or_b64 exec, exec, s[14:15]
	s_and_b32 s14, s3, 3
	v_lshl_or_b32 v80, s14, 14, v10
	s_waitcnt vmcnt(0)
	s_waitcnt lgkmcnt(0)
	s_barrier
	ds_read_b128 v[10:13], v80
	ds_read_b128 v[14:17], v80 offset:1024
	ds_read_b128 v[56:59], v80 offset:8192
	ds_read_b128 v[60:63], v80 offset:9216
	v_and_b32_e32 v98, 31, v0
	v_lshlrev_b32_e32 v82, 2, v98
	s_waitcnt lgkmcnt(2)
	v_mfma_f32_32x32x64_f8f6f4 v[16:31], v[10:17], v[2:9], 0
	ds_read_b128 v[64:67], v80 offset:2048
	ds_read_b128 v[68:71], v80 offset:3072
	ds_read_b128 v[72:75], v80 offset:10240
	ds_read_b128 v[76:79], v80 offset:11264
	s_lshr_b32 s16, s2, 3
	s_lshl_b32 s3, s21, 14
	s_and_b32 s16, s16, 0x1fffffe0
	s_add_i32 s3, s3, s16
	s_lshl_b32 s15, s14, 12
	s_add_i32 s3, s3, s19
	s_lshr_b32 s2, s2, 2
	v_lshrrev_b32_e32 v81, 5, v109
	s_and_b32 s2, s2, 32
	v_lshlrev_b32_e32 v111, 2, v81
	v_lshl_or_b32 v97, s14, 6, v111
	v_lshl_or_b32 v96, v81, 16, v82
	s_load_dwordx2 s[0:1], s[0:1], 0x70
	s_waitcnt lgkmcnt(0)
	v_mfma_f32_32x32x64_f8f6f4 v[0:15], v[56:63], v[2:9], 0
	ds_read_b128 v[88:91], v80 offset:4096
	ds_read_b128 v[92:95], v80 offset:5120
	ds_read_b128 v[114:117], v80 offset:12288
	ds_read_b128 v[118:121], v80 offset:13312
	ds_read_b128 v[100:103], v80 offset:6144
	ds_read_b128 v[104:107], v80 offset:7168
	ds_read_b128 v[56:59], v80 offset:14336
	ds_read_b128 v[60:63], v80 offset:15360
	s_waitcnt lgkmcnt(0)
	s_barrier
	global_load_dword v112, v82, s[8:9]
	global_load_dword v113, v82, s[10:11]
	s_add_i32 s8, s3, s15
	s_mov_b32 s9, 0
	s_lshl_b64 s[8:9], s[8:9], 6
	s_or_b32 s8, s8, s2
	s_lshl_b64 s[2:3], s[8:9], 2
	s_add_u32 s8, s12, s2
	v_lshlrev_b32_e32 v80, 2, v97
	s_addc_u32 s9, s13, s3
	s_lshl_b32 s10, s19, 2
	s_load_dword s4, s[4:5], s10 offset:0x0
	s_nop 0
	s_load_dword s5, s[6:7], s10 offset:0x0
	v_mfma_f32_32x32x64_f8f6f4 v[0:15], v[72:79], v[48:55], v[0:15]
	v_or_b32_e32 v99, 0x10800, v80
	v_or_b32_e32 v123, 0x11000, v80
	v_or_b32_e32 v124, 0x11800, v80
	v_or_b32_e32 v122, 0x10c00, v80
	v_or_b32_e32 v125, 0x11400, v80
	s_mul_i32 s6, s18, 0xa00
	v_mfma_f32_32x32x64_f8f6f4 v[16:31], v[64:71], v[48:55], v[16:31]
	v_or_b32_e32 v48, 0x10000, v80
	v_or_b32_e32 v49, 0x10400, v80
	ds_read_b128 v[52:55], v48
	ds_read_b128 v[84:87], v49
	v_mov_b32_e32 v48, v96
	ds_read_b128 v[64:67], v99
	ds_read_b128 v[68:71], v122
	ds_read_b128 v[72:75], v123
	ds_read_b128 v[76:79], v125
	ds_read_b128 v[80:83], v124
	global_load_dword v110, v48, s[8:9] nt
	v_add_u32_e32 v49, 0x4000, v48
	v_mfma_f32_32x32x64_f8f6f4 v[0:15], v[114:121], v[40:47], v[0:15]
	global_load_dword v120, v49, s[8:9] nt
	s_waitcnt lgkmcnt(0)
	v_mov_b32_e32 v114, s5
	v_mul_f32_e32 v114, 0xbfb8aa3b, v114
	v_mov_b32_e32 v108, 0xbfb8aa3b
	v_mul_f32_e32 v108, s4, v108
	s_nop 1
	v_readfirstlane_b32 s4, v108
	s_nop 1
	v_mfma_f32_32x32x64_f8f6f4 v[16:31], v[88:95], v[40:47], v[16:31]
	s_add_u32 s40, s8, 0x8000
	s_addc_u32 s41, s9, 0
	global_load_dword v121, v48, s[40:41] nt
	s_add_u32 s40, s8, 0xc000
	s_addc_u32 s41, s9, 0
	global_load_dword v126, v48, s[40:41] nt
	v_mfma_f32_32x32x64_f8f6f4 v[16:31], v[100:107], v[32:39], v[16:31]
	s_waitcnt vmcnt(4)
	v_mul_f32_e32 v108, v114, v112
	v_mul_f32_e32 v114, v114, v113
	v_fma_f32 v113, s4, v113, v108
	v_mul_f32_e32 v112, s4, v112
	v_fma_f32 v100, v112, v84, v113
	s_waitcnt vmcnt(4)
	v_fma_f32 v101, v100, v84, v114
	v_or_b32_e32 v84, 8, v97
	v_lshlrev_b32_e32 v102, 2, v84
	v_or_b32_e32 v40, 0x10000, v102
	v_or_b32_e32 v41, 0x10400, v102
	v_or_b32_e32 v104, 0x10800, v102
	v_or_b32_e32 v106, 0x11000, v102
	v_or_b32_e32 v108, 0x11800, v102
	ds_read_b128 v[92:95], v40
	ds_read_b128 v[88:91], v41
	v_or_b32_e32 v105, 0x10c00, v102
	ds_read_b128 v[40:43], v104
	ds_read_b128 v[44:47], v105
	v_mfma_f32_32x32x64_f8f6f4 v[0:15], v[56:63], v[32:39], v[0:15]
	v_mov_b32_e32 v56, v96
	v_or_b32_e32 v107, 0x11400, v102
	ds_read_b128 v[48:51], v106
	ds_read_b128 v[32:35], v107
	ds_read_b128 v[36:39], v108
	v_mov_b32_e32 v58, v101
	s_add_u32 s40, s8, 0x20000
	s_addc_u32 s41, s9, 0
	global_load_dword v57, v56, s[40:41] nt
	s_add_u32 s40, s8, 0x24000
	s_addc_u32 s41, s9, 0
	global_load_dword v59, v56, s[40:41] nt
	s_add_u32 s40, s8, 0x28000
	s_addc_u32 s41, s9, 0
	global_load_dword v60, v56, s[40:41] nt
	v_add_u32_e32 v56, 0x2c000, v56
	global_load_dword v56, v56, s[8:9] nt
	s_add_u32 s40, s8, 0x40000
	s_addc_u32 s41, s9, 0
	global_load_dword v100, v96, s[40:41] nt
	s_add_u32 s40, s8, 0x44000
	s_addc_u32 s41, s9, 0
	global_load_dword v101, v96, s[40:41] nt
	s_add_u32 s40, s8, 0x48000
	s_addc_u32 s41, s9, 0
	global_load_dword v102, v96, s[40:41] nt
	s_add_u32 s40, s8, 0x4c000
	s_addc_u32 s41, s9, 0
	global_load_dword v103, v96, s[40:41] nt
	v_exp_f32_e32 v58, v58
	v_fmamk_f32 v16, v16, 0x39800000, v52
	v_fmamk_f32 v17, v17, 0x39800000, v53
	v_add_f32_e32 v58, 1.0, v58
	v_rcp_f32_e32 v58, v58
	v_fmac_f32_e32 v55, 0x39800000, v19
	s_waitcnt lgkmcnt(5)
	v_fmac_f32_e32 v95, 0x39800000, v23
	s_waitcnt vmcnt(11)
	v_add_f32_e32 v16, v16, v110
	v_mul_f32_e32 v110, v16, v58
	v_fma_f32 v16, v112, v85, v113
	v_fma_f32 v16, v16, v85, v114
	v_exp_f32_e32 v16, v16
	v_fma_f32 v117, v72, v110, 0
	v_fma_f32 v118, v76, v110, 0
	s_waitcnt vmcnt(10)
	v_add_f32_e32 v17, v17, v120
	v_add_f32_e32 v16, 1.0, v16
	v_rcp_f32_e32 v16, v16
	v_fma_f32 v119, v80, v110, 0
	v_fma_f32 v115, v64, v110, 0
	v_fma_f32 v116, v68, v110, 0
	v_mul_f32_e32 v72, v17, v16
	v_fma_f32 v17, v112, v86, v113
	v_fma_f32 v17, v17, v86, v114
	v_exp_f32_e32 v16, v17
	v_fmamk_f32 v17, v18, 0x39800000, v54
	v_fmac_f32_e32 v117, v73, v72
	v_add_f32_e32 v16, 1.0, v16
	v_rcp_f32_e32 v16, v16
	s_waitcnt vmcnt(9)
	v_add_f32_e32 v17, v17, v121
	v_fmac_f32_e32 v118, v77, v72
	v_fmac_f32_e32 v119, v81, v72
	v_mul_f32_e32 v73, v17, v16
	v_fma_f32 v17, v112, v87, v113
	v_fma_f32 v17, v17, v87, v114
	v_exp_f32_e32 v16, v17
	s_waitcnt vmcnt(8)
	v_add_f32_e32 v17, v55, v126
	v_fmac_f32_e32 v117, v74, v73
	v_or_b32_e32 v77, 16, v97
	v_add_f32_e32 v16, 1.0, v16
	v_rcp_f32_e32 v16, v16
	v_fmac_f32_e32 v115, v65, v72
	v_fmac_f32_e32 v116, v69, v72
	v_fmac_f32_e32 v119, v82, v73
	v_mul_f32_e32 v74, v17, v16
	v_fma_f32 v17, v112, v88, v113
	v_fma_f32 v17, v17, v88, v114
	v_fma_f32 v18, v112, v89, v113
	v_fma_f32 v18, v18, v89, v114
	v_exp_f32_e32 v17, v17
	v_exp_f32_e32 v18, v18
	v_add_f32_e32 v17, 1.0, v17
	v_rcp_f32_e32 v17, v17
	v_fmamk_f32 v16, v20, 0x39800000, v92
	v_add_f32_e32 v18, 1.0, v18
	v_rcp_f32_e32 v18, v18
	v_fmac_f32_e32 v117, v75, v74
	v_lshlrev_b32_e32 v52, 2, v77
	v_fmac_f32_e32 v115, v66, v73
	v_fmac_f32_e32 v116, v70, v73
	v_fmac_f32_e32 v118, v78, v73
	v_fmac_f32_e32 v119, v83, v74
	s_waitcnt vmcnt(7)
	v_add_f32_e32 v16, v16, v57
	v_mul_f32_e32 v76, v16, v17
	v_fmamk_f32 v16, v21, 0x39800000, v93
	s_waitcnt vmcnt(6)
	v_add_f32_e32 v16, v16, v59
	v_mul_f32_e32 v75, v16, v18
	v_fmamk_f32 v16, v22, 0x39800000, v94
	s_waitcnt vmcnt(5)
	v_add_f32_e32 v83, v16, v60
	v_fma_f32 v86, v112, v90, v113
	v_fma_f32 v86, v86, v90, v114
	v_or_b32_e32 v16, 0x10000, v52
	v_or_b32_e32 v17, 0x10400, v52
	v_or_b32_e32 v78, 0x10800, v52
	v_or_b32_e32 v80, 0x11000, v52
	v_or_b32_e32 v82, 0x11800, v52
	v_mov_b32_e32 v90, v96
	v_fmac_f32_e32 v115, v67, v74
	v_fmac_f32_e32 v116, v71, v74
	v_fmac_f32_e32 v118, v79, v74
	s_waitcnt vmcnt(4)
	v_add_f32_e32 v87, v95, v56
	v_fma_f32 v89, v112, v91, v113
	v_fma_f32 v89, v89, v91, v114
	ds_read_b128 v[56:59], v16
	ds_read_b128 v[68:71], v17
	v_or_b32_e32 v79, 0x10c00, v52
	ds_read_b128 v[64:67], v78
	ds_read_b128 v[60:63], v79
	v_or_b32_e32 v81, 0x11400, v52
	ds_read_b128 v[16:19], v80
	ds_read_b128 v[20:23], v81
	ds_read_b128 v[52:55], v82
	s_add_u32 s40, s8, 0x60000
	s_addc_u32 s41, s9, 0
	global_load_dword v120, v96, s[40:41] nt
	s_add_u32 s40, s8, 0x64000
	s_addc_u32 s41, s9, 0
	global_load_dword v121, v96, s[40:41] nt
	s_add_u32 s40, s8, 0x68000
	s_addc_u32 s41, s9, 0
	global_load_dword v126, v96, s[40:41] nt
	s_add_u32 s40, s8, 0x6c000
	s_addc_u32 s41, s9, 0
	global_load_dword v92, v96, s[40:41] nt
	s_waitcnt lgkmcnt(8)
	v_fmac_f32_e32 v118, v32, v76
	v_exp_f32_e32 v32, v86
	v_fmac_f32_e32 v118, v33, v75
	v_exp_f32_e32 v33, v89
	v_add_f32_e32 v32, 1.0, v32
	v_rcp_f32_e32 v32, v32
	s_waitcnt lgkmcnt(6)
	v_fmamk_f32 v24, v24, 0x39800000, v56
	v_fmac_f32_e32 v116, v44, v76
	v_fmac_f32_e32 v116, v45, v75
	v_mul_f32_e32 v85, v83, v32
	v_add_f32_e32 v32, 1.0, v33
	v_rcp_f32_e32 v32, v32
	s_waitcnt lgkmcnt(5)
	v_fmac_f32_e32 v118, v34, v85
	v_mul_f32_e32 v83, v87, v32
	v_fma_f32 v32, v112, v68, v113
	v_fma_f32 v32, v32, v68, v114
	v_exp_f32_e32 v32, v32
	v_fma_f32 v33, v112, v69, v113
	v_fma_f32 v33, v33, v69, v114
	v_add_f32_e32 v32, 1.0, v32
	v_rcp_f32_e32 v32, v32
	v_exp_f32_e32 v33, v33
	v_fmac_f32_e32 v116, v46, v85
	v_fmamk_f32 v25, v25, 0x39800000, v57
	v_fmac_f32_e32 v116, v47, v83
	v_fmac_f32_e32 v115, v40, v76
	v_fmac_f32_e32 v115, v41, v75
	v_fmac_f32_e32 v115, v42, v85
	v_fmac_f32_e32 v115, v43, v83
	v_fmac_f32_e32 v59, 0x39800000, v27
	v_fmac_f32_e32 v117, v48, v76
	v_fmac_f32_e32 v119, v36, v76
	v_fmac_f32_e32 v117, v49, v75
	v_fmac_f32_e32 v119, v37, v75
	v_fmac_f32_e32 v117, v50, v85
	v_fmac_f32_e32 v119, v38, v85
	v_fmac_f32_e32 v117, v51, v83
	v_fmac_f32_e32 v118, v35, v83
	v_fmac_f32_e32 v119, v39, v83
	v_mov_b32_e32 v94, v96
	s_waitcnt vmcnt(7)
	v_add_f32_e32 v24, v24, v100
	v_mul_f32_e32 v68, v24, v32
	v_add_f32_e32 v24, 1.0, v33
	v_rcp_f32_e32 v24, v24
	s_waitcnt vmcnt(6)
	v_add_f32_e32 v25, v25, v101
	s_waitcnt lgkmcnt(3)
	v_fmac_f32_e32 v116, v60, v68
	v_mul_f32_e32 v60, v25, v24
	v_fma_f32 v25, v112, v70, v113
	v_fma_f32 v25, v25, v70, v114
	v_exp_f32_e32 v24, v25
	v_fmamk_f32 v25, v26, 0x39800000, v58
	v_fma_f32 v26, v112, v71, v113
	v_fma_f32 v26, v26, v71, v114
	v_add_f32_e32 v24, 1.0, v24
	v_rcp_f32_e32 v24, v24
	v_exp_f32_e32 v26, v26
	s_waitcnt vmcnt(5)
	v_add_f32_e32 v25, v25, v102
	v_fmac_f32_e32 v115, v64, v68
	v_mul_f32_e32 v64, v25, v24
	v_add_f32_e32 v24, 1.0, v26
	v_rcp_f32_e32 v24, v24
	v_fmac_f32_e32 v116, v61, v60
	v_fmac_f32_e32 v116, v62, v64
	s_waitcnt vmcnt(4)
	v_add_f32_e32 v25, v59, v103
	v_or_b32_e32 v62, 24, v97
	v_fmac_f32_e32 v115, v65, v60
	v_mul_f32_e32 v61, v25, v24
	v_lshlrev_b32_e32 v24, 2, v62
	v_fmac_f32_e32 v115, v66, v64
	v_fmac_f32_e32 v116, v63, v61
	v_or_b32_e32 v25, 0x10000, v24
	v_or_b32_e32 v26, 0x10400, v24
	v_or_b32_e32 v63, 0x10800, v24
	v_or_b32_e32 v66, 0x11000, v24
	v_or_b32_e32 v69, 0x11800, v24
	v_mov_b32_e32 v70, v96
	v_fmac_f32_e32 v115, v67, v61
	ds_read_b128 v[48:51], v25
	ds_read_b128 v[56:59], v26
	v_or_b32_e32 v65, 0x10c00, v24
	ds_read_b128 v[44:47], v63
	ds_read_b128 v[32:35], v65
	v_or_b32_e32 v67, 0x11400, v24
	ds_read_b128 v[36:39], v66
	ds_read_b128 v[40:43], v67
	ds_read_b128 v[24:27], v69
	s_waitcnt lgkmcnt(9)
	v_fmac_f32_e32 v117, v16, v68
	s_add_u32 s40, s8, 0x80000
	s_addc_u32 s41, s9, 0
	global_load_dword v95, v96, s[40:41] nt
	v_fmac_f32_e32 v117, v17, v60
	v_fmac_f32_e32 v117, v18, v64
	s_waitcnt lgkmcnt(5)
	v_fma_f32 v18, v112, v56, v113
	v_fma_f32 v17, v18, v56, v114
	v_fmac_f32_e32 v117, v19, v61
	v_fma_f32 v19, v112, v57, v113
	v_fma_f32 v19, v19, v57, v114
	v_exp_f32_e32 v17, v17
	v_exp_f32_e32 v18, v19
	v_add_f32_e32 v17, 1.0, v17
	v_rcp_f32_e32 v17, v17
	v_fmamk_f32 v16, v28, 0x39800000, v48
	v_add_f32_e32 v18, 1.0, v18
	v_rcp_f32_e32 v18, v18
	v_fmac_f32_e32 v51, 0x39800000, v31
	v_fmac_f32_e32 v118, v20, v68
	v_fmac_f32_e32 v119, v52, v68
	v_fmac_f32_e32 v118, v21, v60
	v_fmac_f32_e32 v119, v53, v60
	v_fmac_f32_e32 v118, v22, v64
	v_fmac_f32_e32 v119, v54, v64
	v_fmac_f32_e32 v118, v23, v61
	v_fmac_f32_e32 v119, v55, v61
	s_waitcnt vmcnt(4)
	v_add_f32_e32 v16, v16, v120
	v_mul_f32_e32 v71, v16, v17
	v_fmamk_f32 v16, v29, 0x39800000, v49
	s_waitcnt vmcnt(3)
	v_add_f32_e32 v16, v16, v121
	v_mul_f32_e32 v70, v16, v18
	v_fma_f32 v18, v112, v58, v113
	v_fma_f32 v17, v18, v58, v114
	v_fma_f32 v18, v112, v59, v113
	v_fma_f32 v18, v18, v59, v114
	v_exp_f32_e32 v17, v17
	v_exp_f32_e32 v18, v18
	v_fmamk_f32 v16, v30, 0x39800000, v50
	v_add_f32_e32 v17, 1.0, v17
	v_rcp_f32_e32 v17, v17
	v_add_f32_e32 v18, 1.0, v18
	v_rcp_f32_e32 v18, v18
	s_waitcnt vmcnt(2)
	v_add_f32_e32 v16, v16, v126
	v_mul_f32_e32 v88, v16, v17
	s_waitcnt vmcnt(1)
	v_add_f32_e32 v16, v51, v92
	v_or_b32_e32 v87, 32, v97
	v_mul_f32_e32 v86, v16, v18
	v_lshlrev_b32_e32 v16, 2, v87
	v_or_b32_e32 v17, 0x10000, v16
	v_or_b32_e32 v18, 0x10400, v16
	v_or_b32_e32 v89, 0x10800, v16
	v_or_b32_e32 v91, 0x11000, v16
	v_or_b32_e32 v93, 0x11800, v16
	ds_read_b128 v[28:31], v17
	ds_read_b128 v[100:103], v18
	v_or_b32_e32 v90, 0x10c00, v16
	ds_read_b128 v[52:55], v89
	ds_read_b128 v[48:51], v90
	v_or_b32_e32 v92, 0x11400, v16
	ds_read_b128 v[56:59], v91
	ds_read_b128 v[20:23], v92
	ds_read_b128 v[16:19], v93
	s_waitcnt lgkmcnt(11)
	v_fmac_f32_e32 v115, v44, v71
	s_add_u32 s40, s8, 0x84000
	s_addc_u32 s41, s9, 0
	global_load_dword v44, v94, s[40:41] nt
	v_fmac_f32_e32 v115, v45, v70
	s_add_u32 s40, s8, 0x88000
	s_addc_u32 s41, s9, 0
	global_load_dword v45, v94, s[40:41] nt
	v_fmac_f32_e32 v115, v46, v88
	s_add_u32 s40, s8, 0x8c000
	s_addc_u32 s41, s9, 0
	global_load_dword v46, v94, s[40:41] nt
	s_add_u32 s40, s8, 0xa0000
	s_addc_u32 s41, s9, 0
	global_load_dword v120, v96, s[40:41] nt
	s_add_u32 s40, s8, 0xa4000
	s_addc_u32 s41, s9, 0
	global_load_dword v121, v96, s[40:41] nt
	s_add_u32 s40, s8, 0xa8000
	s_addc_u32 s41, s9, 0
	global_load_dword v126, v96, s[40:41] nt
	s_waitcnt lgkmcnt(7)
	v_fmac_f32_e32 v119, v24, v71
	v_fmac_f32_e32 v119, v25, v70
	s_waitcnt lgkmcnt(5)
	v_fma_f32 v25, v112, v100, v113
	v_fma_f32 v25, v25, v100, v114
	v_exp_f32_e32 v24, v25
	v_fmac_f32_e32 v119, v26, v88
	v_fma_f32 v26, v112, v101, v113
	v_fma_f32 v26, v26, v101, v114
	v_add_f32_e32 v24, 1.0, v24
	v_rcp_f32_e32 v24, v24
	v_exp_f32_e32 v26, v26
	v_fmamk_f32 v0, v0, 0x39800000, v28
	v_fmamk_f32 v1, v1, 0x39800000, v29
	v_fmac_f32_e32 v116, v32, v71
	v_fmac_f32_e32 v117, v36, v71
	v_fmac_f32_e32 v116, v33, v70
	v_fmac_f32_e32 v117, v37, v70
	v_fmac_f32_e32 v116, v34, v88
	v_fmac_f32_e32 v117, v38, v88
	v_fmac_f32_e32 v115, v47, v86
	v_fmac_f32_e32 v116, v35, v86
	v_fmac_f32_e32 v117, v39, v86
	v_fmac_f32_e32 v119, v27, v86
	v_fmac_f32_e32 v31, 0x39800000, v3
	v_or_b32_e32 v27, 40, v97
	v_fmac_f32_e32 v118, v40, v71
	v_lshlrev_b32_e32 v33, 2, v27
	v_fmac_f32_e32 v118, v41, v70
	v_or_b32_e32 v29, 0x10400, v33
	v_fmac_f32_e32 v118, v42, v88
	v_or_b32_e32 v32, 0x11400, v33
	v_fmac_f32_e32 v118, v43, v86
	s_waitcnt vmcnt(6)
	v_add_f32_e32 v0, v0, v95
	v_mul_f32_e32 v25, v0, v24
	v_add_f32_e32 v0, 1.0, v26
	v_rcp_f32_e32 v0, v0
	s_waitcnt vmcnt(5)
	v_add_f32_e32 v1, v1, v44
	s_waitcnt lgkmcnt(4)
	v_fmac_f32_e32 v115, v52, v25
	v_mul_f32_e32 v24, v1, v0
	v_fma_f32 v1, v112, v102, v113
	v_fma_f32 v1, v1, v102, v114
	v_exp_f32_e32 v0, v1
	v_fmamk_f32 v1, v2, 0x39800000, v30
	v_fma_f32 v2, v112, v103, v113
	v_fma_f32 v2, v2, v103, v114
	s_add_u32 s40, s8, 0xac000
	s_addc_u32 s41, s9, 0
	global_load_dword v103, v96, s[40:41] nt
	v_add_f32_e32 v0, 1.0, v0
	v_rcp_f32_e32 v0, v0
	v_exp_f32_e32 v2, v2
	s_waitcnt vmcnt(5)
	v_add_f32_e32 v1, v1, v45
	s_waitcnt lgkmcnt(3)
	v_fmac_f32_e32 v116, v48, v25
	v_mul_f32_e32 v28, v1, v0
	v_add_f32_e32 v0, 1.0, v2
	v_rcp_f32_e32 v0, v0
	s_waitcnt lgkmcnt(2)
	v_fmac_f32_e32 v117, v56, v25
	s_waitcnt vmcnt(4)
	v_add_f32_e32 v1, v31, v46
	v_fmac_f32_e32 v115, v53, v24
	v_fmac_f32_e32 v116, v49, v24
	v_fmac_f32_e32 v117, v57, v24
	v_mul_f32_e32 v26, v1, v0
	v_or_b32_e32 v0, 0x10000, v33
	v_fmac_f32_e32 v115, v54, v28
	v_fmac_f32_e32 v116, v50, v28
	v_fmac_f32_e32 v117, v58, v28
	ds_read_b128 v[0:3], v0
	ds_read_b128 v[34:37], v29
	v_or_b32_e32 v29, 0x10800, v33
	v_or_b32_e32 v30, 0x10c00, v33
	v_or_b32_e32 v31, 0x11000, v33
	v_or_b32_e32 v33, 0x11800, v33
	v_mov_b32_e32 v58, v96
	v_fmac_f32_e32 v115, v55, v26
	v_fmac_f32_e32 v116, v51, v26
	v_fmac_f32_e32 v117, v59, v26
	ds_read_b128 v[38:41], v29
	ds_read_b128 v[42:45], v30
	ds_read_b128 v[46:49], v31
	ds_read_b128 v[50:53], v32
	ds_read_b128 v[54:57], v33
	s_waitcnt lgkmcnt(8)
	v_fmac_f32_e32 v118, v20, v25
	s_add_u32 s40, s8, 0xc4000
	s_addc_u32 s41, s9, 0
	global_load_dword v100, v96, s[40:41] nt
	s_add_u32 s40, s8, 0xc8000
	s_addc_u32 s41, s9, 0
	global_load_dword v101, v96, s[40:41] nt
	s_add_u32 s40, s8, 0xcc000
	s_addc_u32 s41, s9, 0
	global_load_dword v102, v96, s[40:41] nt
	v_fmac_f32_e32 v118, v21, v24
	s_waitcnt lgkmcnt(5)
	v_fma_f32 v21, v112, v34, v113
	v_fma_f32 v21, v21, v34, v114
	v_exp_f32_e32 v20, v21
	v_fmac_f32_e32 v119, v16, v25
	v_fmamk_f32 v0, v4, 0x39800000, v0
	v_add_f32_e32 v16, 1.0, v20
	v_rcp_f32_e32 v16, v16
	v_fmamk_f32 v1, v5, 0x39800000, v1
	v_fmac_f32_e32 v118, v22, v28
	v_fmac_f32_e32 v3, 0x39800000, v7
	v_or_b32_e32 v34, 48, v97
	v_fmac_f32_e32 v118, v23, v26
	v_fmac_f32_e32 v119, v17, v24
	v_fmac_f32_e32 v119, v18, v28
	v_fmac_f32_e32 v119, v19, v26
	s_waitcnt vmcnt(6)
	v_add_f32_e32 v0, v0, v120
	v_mul_f32_e32 v20, v0, v16
	v_fma_f32 v0, v112, v35, v113
	v_fma_f32 v0, v0, v35, v114
	v_exp_f32_e32 v0, v0
	s_waitcnt vmcnt(5)
	v_add_f32_e32 v1, v1, v121
	s_waitcnt lgkmcnt(4)
	v_fmac_f32_e32 v115, v38, v20
	s_waitcnt lgkmcnt(3)
	v_fmac_f32_e32 v116, v42, v20
	v_add_f32_e32 v0, 1.0, v0
	v_rcp_f32_e32 v0, v0
	s_waitcnt lgkmcnt(0)
	v_fmac_f32_e32 v119, v54, v20
	v_fmac_f32_e32 v117, v46, v20
	v_fmac_f32_e32 v118, v50, v20
	v_mul_f32_e32 v21, v1, v0
	v_fma_f32 v1, v112, v36, v113
	v_fma_f32 v1, v1, v36, v114
	v_exp_f32_e32 v0, v1
	v_fmamk_f32 v1, v6, 0x39800000, v2
	s_waitcnt vmcnt(4)
	v_add_f32_e32 v1, v1, v126
	v_fmac_f32_e32 v115, v39, v21
	v_add_f32_e32 v0, 1.0, v0
	v_rcp_f32_e32 v0, v0
	v_lshlrev_b32_e32 v39, 2, v34
	v_fmac_f32_e32 v116, v43, v21
	v_or_b32_e32 v4, 0x10400, v39
	v_mul_f32_e32 v22, v1, v0
	v_fma_f32 v1, v112, v37, v113
	v_fma_f32 v1, v1, v37, v114
	v_exp_f32_e32 v0, v1
	s_waitcnt vmcnt(3)
	v_add_f32_e32 v1, v3, v103
	s_add_u32 s40, s8, 0xc0000
	s_addc_u32 s41, s9, 0
	global_load_dword v103, v96, s[40:41] nt
	v_fmac_f32_e32 v115, v40, v22
	v_fmac_f32_e32 v119, v55, v21
	v_add_f32_e32 v0, 1.0, v0
	v_rcp_f32_e32 v0, v0
	v_fmac_f32_e32 v117, v47, v21
	v_fmac_f32_e32 v118, v51, v21
	v_fmac_f32_e32 v119, v56, v22
	v_mul_f32_e32 v23, v1, v0
	v_or_b32_e32 v0, 0x10000, v39
	v_fmac_f32_e32 v115, v41, v23
	ds_read_b128 v[0:3], v0
	ds_read_b128 v[40:43], v4
	v_fmac_f32_e32 v116, v44, v22
	v_fmac_f32_e32 v117, v48, v22
	v_fmac_f32_e32 v118, v52, v22
	v_fmac_f32_e32 v119, v57, v23
	v_or_b32_e32 v35, 0x10800, v39
	v_or_b32_e32 v36, 0x10c00, v39
	v_or_b32_e32 v37, 0x11000, v39
	v_or_b32_e32 v38, 0x11400, v39
	s_waitcnt lgkmcnt(0)
	v_fma_f32 v58, v112, v41, v113
	v_fma_f32 v58, v58, v41, v114
	v_or_b32_e32 v41, 0x11800, v39
	v_mov_b32_e32 v39, v96
	v_fmac_f32_e32 v116, v45, v23
	v_fmac_f32_e32 v117, v49, v23
	v_fmac_f32_e32 v118, v53, v23
	ds_read_b128 v[16:19], v35
	ds_read_b128 v[4:7], v36
	v_fma_f32 v94, v112, v42, v113
	v_fma_f32 v94, v94, v42, v114
	ds_read_b128 v[44:47], v37
	ds_read_b128 v[48:51], v38
	ds_read_b128 v[52:55], v41
	s_add_u32 s40, s8, 0xe0000
	s_addc_u32 s41, s9, 0
	global_load_dword v120, v96, s[40:41] nt
	s_add_u32 s40, s8, 0xe4000
	s_addc_u32 s41, s9, 0
	global_load_dword v121, v96, s[40:41] nt
	s_add_u32 s40, s8, 0xe8000
	s_addc_u32 s41, s9, 0
	global_load_dword v126, v96, s[40:41] nt
	v_fma_f32 v40, v112, v40, v113
	v_fma_f32 v40, v40, v40, v114
	v_fmamk_f32 v0, v8, 0x39800000, v0
	v_exp_f32_e32 v8, v40
	v_fma_f32 v43, v112, v43, v113
	v_fma_f32 v43, v43, v43, v114
	v_fmac_f32_e32 v3, 0x39800000, v11
	v_add_f32_e32 v8, 1.0, v8
	v_rcp_f32_e32 v8, v8
	s_waitcnt vmcnt(3)
	v_add_f32_e32 v0, v0, v103
	s_add_u32 s40, s8, 0xec000
	s_addc_u32 s41, s9, 0
	global_load_dword v103, v96, s[40:41] nt
	v_mul_f32_e32 v42, v0, v8
	v_fmamk_f32 v0, v9, 0x39800000, v1
	v_exp_f32_e32 v1, v58
	v_add_f32_e32 v0, v0, v100
	s_waitcnt lgkmcnt(4)
	v_fmac_f32_e32 v115, v16, v42
	s_waitcnt lgkmcnt(2)
	v_fmac_f32_e32 v117, v44, v42
	v_add_f32_e32 v1, 1.0, v1
	v_rcp_f32_e32 v1, v1
	s_waitcnt lgkmcnt(1)
	v_fmac_f32_e32 v118, v48, v42
	v_or_b32_e32 v44, 56, v97
	v_fmac_f32_e32 v116, v4, v42
	v_mul_f32_e32 v40, v0, v1
	v_exp_f32_e32 v1, v94
	v_fmamk_f32 v0, v10, 0x39800000, v2
	v_add_f32_e32 v0, v0, v101
	v_fmac_f32_e32 v115, v17, v40
	v_add_f32_e32 v1, 1.0, v1
	v_rcp_f32_e32 v1, v1
	v_fmac_f32_e32 v118, v49, v40
	v_lshlrev_b32_e32 v49, 2, v44
	v_or_b32_e32 v4, 0x10400, v49
	v_mul_f32_e32 v39, v0, v1
	v_exp_f32_e32 v0, v43
	v_add_f32_e32 v1, v3, v102
	v_fmac_f32_e32 v115, v18, v39
	s_waitcnt lgkmcnt(0)
	v_fmac_f32_e32 v119, v52, v42
	v_add_f32_e32 v0, 1.0, v0
	v_rcp_f32_e32 v0, v0
	v_fmac_f32_e32 v117, v45, v40
	v_fmac_f32_e32 v116, v5, v40
	v_fmac_f32_e32 v119, v53, v40
	v_mul_f32_e32 v43, v1, v0
	v_or_b32_e32 v0, 0x10000, v49
	v_fmac_f32_e32 v115, v19, v43
	ds_read_b128 v[0:3], v0
	ds_read_b128 v[16:19], v4
	v_fmac_f32_e32 v117, v46, v39
	v_fmac_f32_e32 v116, v6, v39
	v_fmac_f32_e32 v118, v50, v39
	v_fmac_f32_e32 v119, v54, v39
	v_fmac_f32_e32 v117, v47, v43
	v_or_b32_e32 v45, 0x10800, v49
	v_or_b32_e32 v46, 0x10c00, v49
	v_or_b32_e32 v47, 0x11000, v49
	v_or_b32_e32 v48, 0x11400, v49
	v_or_b32_e32 v49, 0x11800, v49
	v_mov_b32_e32 v58, v96
	v_fmac_f32_e32 v116, v7, v43
	v_fmac_f32_e32 v118, v51, v43
	v_fmac_f32_e32 v119, v55, v43
	ds_read_b128 v[8:11], v45
	ds_read_b128 v[4:7], v46
	s_waitcnt lgkmcnt(3)
	v_fmamk_f32 v0, v12, 0x39800000, v0
	v_fmamk_f32 v1, v13, 0x39800000, v1
	v_fmamk_f32 v2, v14, 0x39800000, v2
	v_fmac_f32_e32 v3, 0x39800000, v15
	ds_read_b128 v[12:15], v47
	ds_read_b128 v[50:53], v48
	ds_read_b128 v[54:57], v49
	s_waitcnt lgkmcnt(5)
	v_fma_f32 v16, v112, v16, v113
	v_fma_f32 v16, v16, v16, v114
	v_exp_f32_e32 v16, v16
	s_waitcnt vmcnt(3)
	v_add_f32_e32 v0, v0, v120
	v_add_f32_e32 v16, 1.0, v16
	v_rcp_f32_e32 v16, v16
	s_waitcnt vmcnt(2)
	v_add_f32_e32 v1, v1, v121
	v_mul_f32_e32 v16, v0, v16
	v_fma_f32 v17, v112, v17, v113
	v_fma_f32 v17, v17, v17, v114
	v_exp_f32_e32 v0, v17
	s_waitcnt lgkmcnt(4)
	v_fmac_f32_e32 v115, v8, v16
	s_waitcnt lgkmcnt(3)
	v_fmac_f32_e32 v116, v4, v16
	s_waitcnt lgkmcnt(2)
	v_fmac_f32_e32 v117, v12, v16
	v_add_f32_e32 v0, 1.0, v0
	v_rcp_f32_e32 v0, v0
	s_waitcnt lgkmcnt(1)
	v_fmac_f32_e32 v118, v50, v16
	s_waitcnt lgkmcnt(0)
	v_fmac_f32_e32 v119, v54, v16
	v_mul_f32_e32 v17, v1, v0
	v_fma_f32 v1, v112, v18, v113
	v_fma_f32 v1, v1, v18, v114
	v_exp_f32_e32 v0, v1
	s_waitcnt vmcnt(1)
	v_add_f32_e32 v1, v2, v126
	v_fma_f32 v113, v112, v19, v113
	v_add_f32_e32 v0, 1.0, v0
	v_rcp_f32_e32 v0, v0
	v_fmac_f32_e32 v115, v9, v17
	v_fmac_f32_e32 v116, v5, v17
	v_fmac_f32_e32 v117, v13, v17
	v_mul_f32_e32 v18, v1, v0
	v_fma_f32 v0, v113, v19, v114
	v_exp_f32_e32 v0, v0
	s_waitcnt vmcnt(0)
	v_add_f32_e32 v1, v3, v103
	v_fmac_f32_e32 v118, v51, v17
	v_fmac_f32_e32 v119, v55, v17
	v_add_f32_e32 v0, 1.0, v0
	v_rcp_f32_e32 v0, v0
	v_fmac_f32_e32 v115, v10, v18
	v_fmac_f32_e32 v116, v6, v18
	v_fmac_f32_e32 v117, v14, v18
	v_mul_f32_e32 v19, v1, v0
	v_mbcnt_lo_u32_b32 v0, -1, 0
	v_mbcnt_hi_u32_b32 v0, -1, v0
	v_and_b32_e32 v2, 64, v0
	v_xor_b32_e32 v1, 32, v0
	v_add_u32_e32 v2, 64, v2
	v_cmp_lt_i32_e32 vcc, v1, v2
	v_fmac_f32_e32 v118, v52, v18
	v_fmac_f32_e32 v119, v56, v18
	v_cndmask_b32_e32 v0, v0, v1, vcc
	v_fmac_f32_e32 v115, v11, v19
	v_fmac_f32_e32 v116, v7, v19
	v_fmac_f32_e32 v117, v15, v19
	v_fmac_f32_e32 v118, v53, v19
	v_fmac_f32_e32 v119, v57, v19
	v_lshlrev_b32_e32 v50, 2, v0
	ds_bpermute_b32 v0, v50, v115
	ds_bpermute_b32 v1, v50, v116
	ds_bpermute_b32 v2, v50, v117
	ds_bpermute_b32 v3, v50, v118
	ds_bpermute_b32 v4, v50, v119
	v_cmp_gt_u32_e32 vcc, 32, v109
	s_and_saveexec_b64 s[4:5], vcc
	s_cbranch_execz .LBB13_8
	s_mul_i32 s7, s14, 0x280
	s_add_i32 s7, s6, s7
	s_waitcnt lgkmcnt(3)
	v_add_f32_e32 v1, v116, v1
	v_add_f32_e32 v0, v115, v0
	v_lshl_or_b32 v5, v98, 2, s7
	s_waitcnt lgkmcnt(0)
	v_add_f32_e32 v4, v119, v4
	v_add_f32_e32 v3, v118, v3
	v_add_f32_e32 v2, v117, v2
	ds_write2_b32 v5, v0, v1 offset1:32
	ds_write2_b32 v5, v2, v3 offset0:64 offset1:96
	ds_write_b32 v5, v4 offset:512
